# speedup vs baseline: 1.0033x; 1.0033x over previous
_Z10attn64_fwdPKtS0_S0_Pt8PrepArgs:
	s_mov_b64 s[4:5], -1
	s_cmpk_lt_u32 s2, 0x300
	v_lshlrev_b32_e32 v1, 4, v0
	s_cbranch_scc0 .LBB1_53
	s_lshr_b32 s12, s2, 4
	s_and_b32 s3, s2, 7
	s_and_b32 s12, s12, 56
	s_or_b32 s3, s12, s3
	s_mul_i32 s12, s3, 43
	s_lshr_b32 s14, s12, 9
	s_mul_i32 s12, s14, 12
	v_readfirstlane_b32 s15, v0
	s_lshl_b32 s13, s2, 4
	s_load_dwordx8 s[4:11], s[0:1], 0x0
	s_sub_i32 s3, s3, s12
	s_lshr_b32 s24, s15, 6
	s_lshl_b32 s12, s14, 11
	s_and_b32 s13, s13, 0x780
	s_or_b32 s12, s12, s13
	s_lshl_b32 s13, s24, 5
	s_add_i32 s12, s12, s13
	s_mul_hi_u32 s13, s12, 0x300
	s_mulk_i32 s12, 0x300
	s_lshl_b64 s[12:13], s[12:13], 1
	s_waitcnt lgkmcnt(0)
	s_add_u32 s4, s4, s12
	s_addc_u32 s5, s5, s13
	s_and_b32 s16, s3, 0xff
	s_lshl_b32 s3, s16, 6
	s_lshl_b32 s17, s16, 7
	s_add_u32 s18, s4, s17
	s_addc_u32 s19, s5, 0
	s_and_b32 s16, s15, 0x3fffffc0
	s_mul_i32 s14, s14, 0x300000
	s_add_u32 s4, s6, s14
	v_and_b32_e32 v212, 63, v0
	s_addc_u32 s5, s7, 0
	s_add_u32 s4, s4, s17
	v_mul_u32_u24_e32 v2, 0x300, v212
	s_addc_u32 s5, s5, 0
	v_lshlrev_b32_e32 v200, 1, v2
	v_mov_b32_e32 v201, 0
	s_lshl_b32 s20, s24, 4
	v_lshl_add_u64 v[2:3], s[4:5], 0, v[200:201]
	s_add_u32 s4, s8, s14
	s_addc_u32 s5, s9, 0
	s_mov_b32 s21, 0
	s_add_u32 s4, s4, s17
	v_lshl_add_u64 v[198:199], v[2:3], 0, s[20:21]
	s_addc_u32 s5, s5, 0
	v_bfe_u32 v2, v0, 2, 4
	s_lshr_b32 s6, s15, 2
	v_and_or_b32 v2, s6, 48, v2
	v_mul_u32_u24_e32 v2, 0x300, v2
	s_and_b32 s20, s6, 0x3fffffc0
	s_lshl_b32 s27, s24, 10
	v_lshlrev_b32_e32 v200, 1, v2
	s_cmp_lg_u32 0, -1
	v_lshl_add_u64 v[2:3], s[4:5], 0, v[200:201]
	v_lshlrev_b32_e32 v213, 3, v0
	s_cselect_b32 s4, 0, 0
	v_and_b32_e32 v50, 24, v213
	s_add_i32 s29, s27, s4
	s_mov_b32 s4, m0
	s_mov_b32 m0, s29
	s_nop 0
	global_load_lds_dwordx4 v[198:199], off
	s_mov_b32 m0, s4
	v_lshl_add_u64 v[2:3], v[2:3], 0, s[20:21]
	v_lshlrev_b32_e32 v200, 1, v50
	v_lshl_add_u64 v[194:195], v[198:199], 0, 64
	s_add_i32 s28, s29, 0x1000
	s_mov_b32 s4, m0
	s_mov_b32 m0, s28
	s_nop 0
	global_load_lds_dwordx4 v[194:195], off
	s_mov_b32 m0, s4
	v_lshl_add_u64 v[202:203], v[2:3], 0, v[200:201]
	s_add_i32 s26, s29, 0x6000
	s_mov_b32 s4, m0
	s_mov_b32 m0, s26
	s_nop 0
	global_load_lds_dwordx4 v[202:203], off
	s_mov_b32 m0, s4
	v_lshl_add_u64 v[196:197], v[202:203], 0, 64
	s_add_i32 s25, s29, 0x7000
	s_mov_b32 s4, m0
	s_mov_b32 m0, s25
	s_nop 0
	global_load_lds_dwordx4 v[196:197], off
	s_mov_b32 m0, s4
	s_mov_b64 s[4:5], 0x18000
	v_lshl_add_u64 v[2:3], v[198:199], 0, s[4:5]
	s_mov_b64 s[14:15], 0x18040
	v_and_b32_e32 v214, 31, v0
	v_bfe_u32 v215, v0, 5, 1
	s_add_i32 s6, s29, 0x2000
	s_mov_b32 s7, m0
	s_mov_b32 m0, s6
	s_nop 0
	global_load_lds_dwordx4 v[2:3], off
	s_mov_b32 m0, s7
	v_lshl_add_u64 v[2:3], v[198:199], 0, s[14:15]
	s_add_i32 s6, s29, 0x3000
	s_mov_b32 s7, m0
	s_mov_b32 m0, s6
	s_nop 0
	global_load_lds_dwordx4 v[2:3], off
	s_mov_b32 m0, s7
	v_mul_u32_u24_e32 v2, 0x300, v214
	v_lshlrev_b32_e32 v200, 4, v215
	v_lshl_or_b32 v2, v2, 1, v200
	global_load_dwordx4 v[174:177], v2, s[18:19]
	global_load_dwordx4 v[170:173], v2, s[18:19] offset:32
	global_load_dwordx4 v[166:169], v2, s[18:19] offset:64
	global_load_dwordx4 v[162:165], v2, s[18:19] offset:96
	s_mov_b64 s[6:7], 0x30000
	s_mov_b64 s[8:9], 0x30040
	v_lshlrev_b32_e32 v2, 10, v215
	v_lshlrev_b32_e32 v3, 4, v214
	v_add3_u32 v218, 0, v2, v3
	v_lshl_add_u64 v[2:3], v[198:199], 0, s[6:7]
	v_lshl_add_u64 v[4:5], v[198:199], 0, s[8:9]
	s_add_i32 s8, s29, 0x4000
	s_mov_b32 s17, m0
	s_mov_b32 m0, s8
	s_nop 0
	global_load_lds_dwordx4 v[2:3], off
	s_mov_b32 m0, s17
	s_add_i32 s9, s29, 0x5000
	s_mov_b32 s8, m0
	s_mov_b32 m0, s9
	s_nop 0
	global_load_lds_dwordx4 v[4:5], off
	s_mov_b32 m0, s8
	s_waitcnt vmcnt(6) lgkmcnt(0)
	s_barrier
	ds_read_b128 v[2:5], v218
	ds_read_b128 v[6:9], v218 offset:512
	ds_read_b128 v[34:37], v218 offset:2048
	ds_read_b128 v[38:41], v218 offset:2560
	s_mov_b64 s[8:9], 0x48000
	s_mov_b64 s[18:19], 0x48040
	s_mov_b32 s31, -1
	s_movk_i32 s35, 0x2000
	s_movk_i32 s33, 0x4000
	s_mov_b32 s34, 0x41000000
	s_waitcnt vmcnt(3) lgkmcnt(3)
	v_mfma_f32_32x32x16_f16 v[18:33], v[2:5], v[174:177], 0
	s_waitcnt lgkmcnt(2)
	v_mfma_f32_32x32x16_f16 v[2:17], v[6:9], v[174:177], 0
	s_waitcnt vmcnt(2) lgkmcnt(1)
	v_mfma_f32_32x32x16_f16 v[18:33], v[34:37], v[170:173], v[18:33]
	s_waitcnt lgkmcnt(0)
	v_mfma_f32_32x32x16_f16 v[2:17], v[38:41], v[170:173], v[2:17]
	ds_read_b128 v[34:37], v218 offset:4096
	ds_read_b128 v[38:41], v218 offset:4608
	s_waitcnt vmcnt(1) lgkmcnt(1)
	v_mfma_f32_32x32x16_f16 v[18:33], v[34:37], v[166:169], v[18:33]
	s_waitcnt lgkmcnt(0)
	v_mfma_f32_32x32x16_f16 v[2:17], v[38:41], v[166:169], v[2:17]
	ds_read_b128 v[34:37], v218 offset:6144
	ds_read_b128 v[38:41], v218 offset:6656
	s_waitcnt vmcnt(0) lgkmcnt(1)
	v_mfma_f32_32x32x16_f16 v[18:33], v[34:37], v[162:165], v[18:33]
	s_waitcnt lgkmcnt(0)
	v_mfma_f32_32x32x16_f16 v[2:17], v[38:41], v[162:165], v[2:17]
	s_nop 9
	v_max_f32_e32 v34, v19, v19
	v_max_f32_e32 v35, v18, v18
	v_max_f32_e32 v34, v35, v34
	v_max3_f32 v36, v20, v21, v3
	v_max3_f32 v34, v34, v2, v4
	v_max3_f32 v35, v36, v24, v25
	v_max3_f32 v34, v34, v5, v22
	v_max3_f32 v35, v35, v8, v9
	v_max3_f32 v34, v34, v23, v6
	v_max3_f32 v35, v35, v28, v29
	v_max3_f32 v34, v34, v7, v26
	v_max3_f32 v35, v35, v12, v13
	v_max3_f32 v34, v34, v27, v10
	v_max3_f32 v35, v35, v32, v33
	v_max3_f32 v34, v34, v11, v30
	v_max3_f32 v35, v35, v16, v17
	v_max3_f32 v34, v34, v31, v14
	v_max3_f32 v34, v34, v15, v35
	v_mov_b32_e32 v35, v34
	s_nop 1
	v_permlane32_swap_b32_e32 v34, v35
	v_max_f32_e32 v35, v35, v35
	v_max_f32_e32 v34, v34, v34
	v_max_f32_e32 v219, v34, v35
	v_xor_b32_e32 v34, 0x80000000, v219
	v_mov_b32_e32 v35, v34
	v_mov_b32_e32 v36, v34
	v_mov_b32_e32 v37, v34
	v_mov_b32_e32 v38, v34
	v_mov_b32_e32 v39, v34
	v_mov_b32_e32 v40, v34
	v_mov_b32_e32 v41, v34
	v_mov_b32_e32 v42, v34
	v_mov_b32_e32 v43, v34
	v_mov_b32_e32 v44, v34
	v_mov_b32_e32 v45, v34
	v_mov_b32_e32 v46, v34
	v_mov_b32_e32 v47, v34
	v_mov_b32_e32 v48, v34
	v_mov_b32_e32 v49, v34
	s_waitcnt vmcnt(0) lgkmcnt(0)
	s_barrier
	v_sub_f32_e32 v51, v2, v219
	v_sub_f32_e32 v52, v3, v219
	v_lshl_add_u64 v[2:3], v[198:199], 0, s[8:9]
	s_mov_b32 s17, m0
	s_mov_b32 m0, s29
	s_nop 0
	global_load_lds_dwordx4 v[2:3], off
	s_mov_b32 m0, s17
	v_lshl_add_u64 v[2:3], v[198:199], 0, s[18:19]
	s_mov_b32 s17, m0
	s_mov_b32 m0, s28
	s_nop 0
	global_load_lds_dwordx4 v[2:3], off
	s_mov_b32 m0, s17
	s_add_i32 s17, s29, 0x8000
	v_lshl_add_u64 v[2:3], v[202:203], 0, s[4:5]
	s_mov_b32 s4, m0
	s_mov_b32 m0, s17
	s_nop 0
	global_load_lds_dwordx4 v[2:3], off
	s_mov_b32 m0, s4
	s_add_i32 s4, s29, 0x9000
	v_lshl_add_u64 v[2:3], v[202:203], 0, s[14:15]
	s_mov_b32 s5, m0
	s_mov_b32 m0, s4
	s_nop 0
	global_load_lds_dwordx4 v[2:3], off
	s_mov_b32 m0, s5
	ds_read_b128 v[82:85], v218 offset:8192
	ds_read_b128 v[182:185], v218 offset:8704
	ds_read_b128 v[178:181], v218 offset:10240
	ds_read_b128 v[142:145], v218 offset:10752
	ds_read_b128 v[138:141], v218 offset:12288
	ds_read_b128 v[134:137], v218 offset:12800
	ds_read_b128 v[130:133], v218 offset:14336
	ds_read_b128 v[126:129], v218 offset:14848
	v_lshlrev_b32_e32 v2, 1, v0
	v_and_b32_e32 v2, 32, v2
	v_sub_f32_e32 v18, v18, v219
	v_sub_f32_e32 v19, v19, v219
	v_sub_f32_e32 v20, v20, v219
	v_sub_f32_e32 v21, v21, v219
	v_sub_f32_e32 v22, v22, v219
	v_sub_f32_e32 v23, v23, v219
	v_sub_f32_e32 v24, v24, v219
	v_sub_f32_e32 v25, v25, v219
	v_sub_f32_e32 v26, v26, v219
	v_sub_f32_e32 v27, v27, v219
	v_sub_f32_e32 v28, v28, v219
	v_sub_f32_e32 v29, v29, v219
	v_sub_f32_e32 v30, v30, v219
	v_sub_f32_e32 v31, v31, v219
	v_sub_f32_e32 v32, v32, v219
	v_sub_f32_e32 v33, v33, v219
	v_sub_f32_e32 v4, v4, v219
	v_sub_f32_e32 v5, v5, v219
	v_sub_f32_e32 v6, v6, v219
	v_sub_f32_e32 v7, v7, v219
	v_sub_f32_e32 v8, v8, v219
	v_sub_f32_e32 v9, v9, v219
	v_sub_f32_e32 v10, v10, v219
	v_sub_f32_e32 v11, v11, v219
	v_sub_f32_e32 v12, v12, v219
	v_sub_f32_e32 v13, v13, v219
	v_sub_f32_e32 v14, v14, v219
	v_sub_f32_e32 v15, v15, v219
	v_sub_f32_e32 v16, v16, v219
	v_sub_f32_e32 v17, v17, v219
	v_add3_u32 v2, 0, v2, v50
	v_lshlrev_b32_e32 v3, 8, v215
	v_and_b32_e32 v50, 0xc0, v1
	v_add3_u32 v216, v2, v3, v50
	v_exp_f32_e32 v66, v18
	v_exp_f32_e32 v67, v19
	v_exp_f32_e32 v50, v51
	v_exp_f32_e32 v51, v52
	v_exp_f32_e32 v68, v20
	v_exp_f32_e32 v52, v4
	v_exp_f32_e32 v69, v21
	v_exp_f32_e32 v53, v5
	v_exp_f32_e32 v70, v22
	v_exp_f32_e32 v54, v6
	v_exp_f32_e32 v71, v23
	v_exp_f32_e32 v55, v7
	v_exp_f32_e32 v72, v24
	v_exp_f32_e32 v56, v8
	v_exp_f32_e32 v73, v25
	v_exp_f32_e32 v57, v9
	v_exp_f32_e32 v74, v26
	v_exp_f32_e32 v58, v10
	v_exp_f32_e32 v75, v27
	v_exp_f32_e32 v59, v11
	v_exp_f32_e32 v76, v28
	v_exp_f32_e32 v60, v12
	v_exp_f32_e32 v77, v29
	v_exp_f32_e32 v61, v13
	v_exp_f32_e32 v78, v30
	v_exp_f32_e32 v62, v14
	v_exp_f32_e32 v79, v31
	v_exp_f32_e32 v63, v15
	v_exp_f32_e32 v80, v32
	v_exp_f32_e32 v64, v16
	v_exp_f32_e32 v81, v33
	v_exp_f32_e32 v65, v17
	s_lshl_b32 s4, s16, 2
	s_waitcnt vmcnt(4) lgkmcnt(0)
	s_barrier
	s_add_i32 s30, s4, 0
	v_cmp_gt_u32_e64 s[4:5], 32, v212
	s_mov_b64 s[14:15], 0
	s_mov_b64 s[16:17], 0x60000
	s_mov_b64 s[18:19], 0x78000
	v_mov_b32_e32 v2, v201
	v_mov_b32_e32 v3, v201
	v_mov_b32_e32 v4, v201
	v_mov_b32_e32 v5, v201
	v_mov_b32_e32 v6, v201
	v_mov_b32_e32 v7, v201
	v_mov_b32_e32 v8, v201
	v_mov_b32_e32 v9, v201
	v_mov_b32_e32 v10, v201
	v_mov_b32_e32 v11, v201
	v_mov_b32_e32 v12, v201
	v_mov_b32_e32 v13, v201
	v_mov_b32_e32 v14, v201
	v_mov_b32_e32 v15, v201
	v_mov_b32_e32 v16, v201
	v_mov_b32_e32 v17, v201
	v_mov_b32_e32 v18, v201
	v_mov_b32_e32 v19, v201
	v_mov_b32_e32 v20, v201
	v_mov_b32_e32 v21, v201
	v_mov_b32_e32 v22, v201
	v_mov_b32_e32 v23, v201
	v_mov_b32_e32 v24, v201
	v_mov_b32_e32 v25, v201
	v_mov_b32_e32 v26, v201
	v_mov_b32_e32 v27, v201
	v_mov_b32_e32 v28, v201
	v_mov_b32_e32 v29, v201
	v_mov_b32_e32 v30, v201
	v_mov_b32_e32 v31, v201
	v_mov_b32_e32 v32, v201
	v_mov_b32_e32 v33, v201
	v_lshl_add_u32 v217, v214, 2, s30
	v_readfirstlane_b32 s40, v198
	v_readfirstlane_b32 s41, v199
	v_readfirstlane_b32 s42, v202
	v_readfirstlane_b32 s43, v203
	s_nop 3
	v_subrev_u32_e32 v221, s40, v198
	v_subrev_u32_e32 v222, s42, v202
	s_add_u32 s44, s40, s16
	s_addc_u32 s45, s41, s17
	s_add_u32 s46, s44, 64
	s_addc_u32 s47, s45, 0
	s_add_u32 s48, s42, s6
	s_addc_u32 s49, s43, s7
	s_add_u32 s50, s48, 64
	s_addc_u32 s51, s49, 0
	s_add_u32 s52, s40, s18
	s_addc_u32 s53, s41, s19
	s_add_u32 s54, s52, 64
	s_addc_u32 s55, s53, 0
	s_add_u32 s56, s42, s8
	s_addc_u32 s57, s43, s9
	s_add_u32 s58, s56, 64
	s_addc_u32 s59, s57, 0

.LBB1_4:
	s_waitcnt lgkmcnt(14)
	v_mfma_f32_32x32x16_f16 v[2:17], v[158:161], v[122:125], v[2:17]
	v_exp_f32_e32 v98, v98
	v_exp_f32_e32 v99, v99
	v_exp_f32_e32 v100, v100
	v_exp_f32_e32 v101, v101
	s_add_i32 m0, s35, s29
	s_nop 0
	global_load_lds_dwordx4 v221, s[44:45]
	s_add_u32 s44, s44, 0x30000
	s_addc_u32 s45, s45, 0
	s_waitcnt lgkmcnt(12)
	v_mfma_f32_32x32x16_f16 v[18:33], v[158:161], v[118:121], v[18:33]
	v_exp_f32_e32 v102, v102
	v_exp_f32_e32 v103, v103
	v_exp_f32_e32 v104, v104
	v_exp_f32_e32 v105, v105
	s_add_i32 m0, s35, s28
	s_nop 0
	global_load_lds_dwordx4 v221, s[46:47]
	s_add_u32 s46, s46, 0x30000
	s_addc_u32 s47, s47, 0
	v_add_u32_e32 v60, s33, v218
	ds_read_b128 v[118:121], v60
	ds_read_b128 v[178:181], v60 offset:512
	s_waitcnt lgkmcnt(12)
	v_mfma_f32_32x32x16_f16 v[2:17], v[154:157], v[114:117], v[2:17]
	v_exp_f32_e32 v106, v106
	v_exp_f32_e32 v107, v107
	v_exp_f32_e32 v108, v108
	v_exp_f32_e32 v109, v109
	s_add_i32 m0, s33, s26
	s_nop 0
	global_load_lds_dwordx4 v222, s[48:49]
	s_add_u32 s48, s48, 0x30000
	s_addc_u32 s49, s49, 0
	ds_read_b128 v[186:189], v60 offset:2048
	ds_read_b128 v[78:81], v60 offset:2560
	s_waitcnt lgkmcnt(12)
	v_mfma_f32_32x32x16_f16 v[18:33], v[154:157], v[74:77], v[18:33]
	v_exp_f32_e32 v110, v110
	v_exp_f32_e32 v111, v111
	v_exp_f32_e32 v112, v112
	v_exp_f32_e32 v113, v113
	s_add_i32 m0, s33, s25
	s_nop 0
	global_load_lds_dwordx4 v222, s[50:51]
	s_add_u32 s50, s50, 0x30000
	s_addc_u32 s51, s51, 0
	ds_read_b128 v[74:77], v60 offset:4096
	ds_read_b128 v[62:65], v60 offset:4608
	s_waitcnt lgkmcnt(12)
	v_mfma_f32_32x32x16_f16 v[2:17], v[150:153], v[70:73], v[2:17]
	v_exp_f32_e32 v82, v82
	v_exp_f32_e32 v83, v83
	v_exp_f32_e32 v84, v84
	v_exp_f32_e32 v85, v85
	ds_read_b128 v[70:73], v60 offset:6144
	ds_read_b128 v[58:61], v60 offset:6656
	s_waitcnt lgkmcnt(12)
	v_mfma_f32_32x32x16_f16 v[18:33], v[150:153], v[66:69], v[18:33]
	v_exp_f32_e32 v86, v86
	v_exp_f32_e32 v87, v87
	v_exp_f32_e32 v88, v88
	v_exp_f32_e32 v89, v89
	s_waitcnt lgkmcnt(10)
	v_mfma_f32_32x32x16_f16 v[2:17], v[146:149], v[54:57], v[2:17]
	v_exp_f32_e32 v90, v90
	v_exp_f32_e32 v91, v91
	v_exp_f32_e32 v92, v92
	v_exp_f32_e32 v93, v93
	s_waitcnt lgkmcnt(8)
	v_mfma_f32_32x32x16_f16 v[18:33], v[146:149], v[50:53], v[18:33]
	v_exp_f32_e32 v94, v94
	v_exp_f32_e32 v95, v95
	v_exp_f32_e32 v96, v96
	v_exp_f32_e32 v97, v97
	s_waitcnt vmcnt(4) lgkmcnt(0)
	s_barrier
	s_andn2_b64 vcc, exec, s[20:21]
	s_cbranch_vccnz .LBB1_6
	v_add_u32_e32 v114, s30, v200
	ds_read_b128 v[50:53], v114 offset:49248
	ds_read_b128 v[54:57], v114 offset:49216
	ds_read_b128 v[66:69], v114 offset:49184
	ds_read_b128 v[114:117], v114 offset:49152
	s_waitcnt lgkmcnt(3)
	v_pk_mul_f32 v[14:15], v[14:15], v[50:51]
	s_waitcnt lgkmcnt(2)
	v_pk_mul_f32 v[10:11], v[10:11], v[54:55]
	s_waitcnt lgkmcnt(1)
	v_pk_mul_f32 v[6:7], v[6:7], v[66:67]
	v_pk_mul_f32 v[16:17], v[16:17], v[52:53]
	v_pk_mul_f32 v[12:13], v[12:13], v[56:57]
	v_pk_mul_f32 v[8:9], v[8:9], v[68:69]
	s_waitcnt lgkmcnt(0)
	v_pk_mul_f32 v[4:5], v[4:5], v[116:117]
	v_pk_mul_f32 v[2:3], v[2:3], v[114:115]
	v_pk_mul_f32 v[30:31], v[30:31], v[50:51]
	v_pk_mul_f32 v[26:27], v[26:27], v[54:55]
	v_pk_mul_f32 v[22:23], v[22:23], v[66:67]
	v_pk_mul_f32 v[32:33], v[32:33], v[52:53]
	v_pk_mul_f32 v[28:29], v[28:29], v[56:57]
	v_pk_mul_f32 v[24:25], v[24:25], v[68:69]
	v_pk_mul_f32 v[20:21], v[20:21], v[116:117]
	v_pk_mul_f32 v[18:19], v[18:19], v[114:115]

.LBB1_10:
	s_add_i32 s22, s33, 0x2000
	s_cmpk_lg_i32 s33, 0x4000
	s_cselect_b32 s35, s22, 0
	s_waitcnt lgkmcnt(14)
	v_mfma_f32_32x32x16_f16 v[2:17], v[158:161], v[190:193], v[2:17]
	v_exp_f32_e32 v66, v130
	v_exp_f32_e32 v67, v131
	v_exp_f32_e32 v68, v132
	v_exp_f32_e32 v69, v133
	s_add_i32 m0, s33, s29
	s_nop 0
	global_load_lds_dwordx4 v221, s[52:53]
	s_add_u32 s52, s52, 0x30000
	s_addc_u32 s53, s53, 0
	s_waitcnt lgkmcnt(12)
	v_mfma_f32_32x32x16_f16 v[18:33], v[158:161], v[182:185], v[18:33]
	v_exp_f32_e32 v78, v142
	v_exp_f32_e32 v79, v143
	v_exp_f32_e32 v80, v144
	v_exp_f32_e32 v81, v145
	s_add_i32 m0, s33, s28
	s_nop 0
	global_load_lds_dwordx4 v221, s[54:55]
	s_add_u32 s54, s54, 0x30000
	s_addc_u32 s55, s55, 0
	v_add_u32_e32 v86, s35, v218
	ds_read_b128 v[82:85], v86
	ds_read_b128 v[182:185], v86 offset:512
	s_waitcnt lgkmcnt(12)
	v_mfma_f32_32x32x16_f16 v[2:17], v[154:157], v[178:181], v[2:17]
	v_exp_f32_e32 v74, v138
	v_exp_f32_e32 v75, v139
	v_exp_f32_e32 v76, v140
	v_exp_f32_e32 v77, v141
	s_add_i32 m0, s35, s26
	s_nop 0
	global_load_lds_dwordx4 v222, s[56:57]
	s_add_u32 s56, s56, 0x30000
	s_addc_u32 s57, s57, 0
	ds_read_b128 v[178:181], v86 offset:2048
	ds_read_b128 v[142:145], v86 offset:2560
	s_waitcnt lgkmcnt(12)
	v_mfma_f32_32x32x16_f16 v[18:33], v[154:157], v[186:189], v[18:33]
	v_exp_f32_e32 v70, v134
	v_exp_f32_e32 v71, v135
	v_exp_f32_e32 v72, v136
	v_exp_f32_e32 v73, v137
	s_add_i32 m0, s35, s25
	s_nop 0
	global_load_lds_dwordx4 v222, s[58:59]
	s_add_u32 s58, s58, 0x30000
	s_addc_u32 s59, s59, 0
	ds_read_b128 v[138:141], v86 offset:4096
	ds_read_b128 v[134:137], v86 offset:4608
	s_waitcnt lgkmcnt(12)
	v_mfma_f32_32x32x16_f16 v[2:17], v[150:153], v[110:113], v[2:17]
	v_exp_f32_e32 v62, v126
	v_exp_f32_e32 v63, v127
	v_exp_f32_e32 v64, v128
	v_exp_f32_e32 v65, v129
	ds_read_b128 v[130:133], v86 offset:6144
	ds_read_b128 v[126:129], v86 offset:6656
	s_waitcnt lgkmcnt(12)
	v_mfma_f32_32x32x16_f16 v[18:33], v[150:153], v[106:109], v[18:33]
	v_exp_f32_e32 v50, v114
	v_exp_f32_e32 v51, v115
	v_exp_f32_e32 v52, v116
	v_exp_f32_e32 v53, v117
	s_waitcnt lgkmcnt(10)
	v_mfma_f32_32x32x16_f16 v[2:17], v[146:149], v[102:105], v[2:17]
	v_exp_f32_e32 v54, v118
	v_exp_f32_e32 v55, v119
	v_exp_f32_e32 v56, v120
	v_exp_f32_e32 v57, v121
	s_waitcnt lgkmcnt(8)
	v_mfma_f32_32x32x16_f16 v[18:33], v[146:149], v[98:101], v[18:33]
	v_exp_f32_e32 v58, v122
	v_exp_f32_e32 v59, v123
	v_exp_f32_e32 v60, v124
	v_exp_f32_e32 v61, v125
	s_waitcnt vmcnt(4) lgkmcnt(0)
	s_barrier
	s_andn2_b64 vcc, exec, s[20:21]
	s_cbranch_vccnz .LBB1_12
	v_add_u32_e32 v98, s30, v200
	ds_read_b128 v[86:89], v98 offset:49248
	ds_read_b128 v[90:93], v98 offset:49216
	ds_read_b128 v[94:97], v98 offset:49152
	ds_read_b128 v[98:101], v98 offset:49184
	s_waitcnt lgkmcnt(3)
	v_pk_mul_f32 v[16:17], v[16:17], v[88:89]
	v_pk_mul_f32 v[14:15], v[14:15], v[86:87]
	s_waitcnt lgkmcnt(2)
	v_pk_mul_f32 v[12:13], v[12:13], v[92:93]
	v_pk_mul_f32 v[10:11], v[10:11], v[90:91]
	s_waitcnt lgkmcnt(0)
	v_pk_mul_f32 v[8:9], v[8:9], v[100:101]
	v_pk_mul_f32 v[6:7], v[6:7], v[98:99]
	v_pk_mul_f32 v[4:5], v[4:5], v[96:97]
	v_pk_mul_f32 v[2:3], v[2:3], v[94:95]
	v_pk_mul_f32 v[32:33], v[32:33], v[88:89]
	v_pk_mul_f32 v[30:31], v[30:31], v[86:87]
	v_pk_mul_f32 v[28:29], v[28:29], v[92:93]
	v_pk_mul_f32 v[26:27], v[26:27], v[90:91]
	v_pk_mul_f32 v[24:25], v[24:25], v[100:101]
	v_pk_mul_f32 v[22:23], v[22:23], v[98:99]
	v_pk_mul_f32 v[20:21], v[20:21], v[96:97]
	v_pk_mul_f32 v[18:19], v[18:19], v[94:95]

	.amdhsa_kernel _Z10attn64_fwdPKtS0_S0_Pt8PrepArgs
		.amdhsa_group_segment_fixed_size 0
		.amdhsa_private_segment_fixed_size 0
		.amdhsa_kernarg_size 176
		.amdhsa_user_sgpr_count 2
		.amdhsa_user_sgpr_dispatch_ptr 0
		.amdhsa_user_sgpr_queue_ptr 0
		.amdhsa_user_sgpr_kernarg_segment_ptr 1
		.amdhsa_user_sgpr_dispatch_id 0
		.amdhsa_user_sgpr_kernarg_preload_length 0
		.amdhsa_user_sgpr_kernarg_preload_offset 0
		.amdhsa_user_sgpr_private_segment_size 0
		.amdhsa_uses_dynamic_stack 0
		.amdhsa_enable_private_segment 0
		.amdhsa_system_sgpr_workgroup_id_x 1
		.amdhsa_system_sgpr_workgroup_id_y 0
		.amdhsa_system_sgpr_workgroup_id_z 0
		.amdhsa_system_sgpr_workgroup_info 0
		.amdhsa_system_vgpr_workitem_id 0
		.amdhsa_next_free_vgpr 223
		.amdhsa_next_free_sgpr 60
		.amdhsa_accum_offset 224
		.amdhsa_reserve_vcc 1
		.amdhsa_float_round_mode_32 0
		.amdhsa_float_round_mode_16_64 0
		.amdhsa_float_denorm_mode_32 3
		.amdhsa_float_denorm_mode_16_64 3
		.amdhsa_dx10_clamp 1
		.amdhsa_ieee_mode 1
		.amdhsa_fp16_overflow 0
		.amdhsa_tg_split 0
		.amdhsa_exception_fp_ieee_invalid_op 0
		.amdhsa_exception_fp_denorm_src 0
		.amdhsa_exception_fp_ieee_div_zero 0
		.amdhsa_exception_fp_ieee_overflow 0
		.amdhsa_exception_fp_ieee_underflow 0
		.amdhsa_exception_fp_ieee_inexact 0
		.amdhsa_exception_int_div_zero 0
	.end_amdhsa_kernel

amdhsa.kernels:
  - .agpr_count:     0
    .args:
      - .offset:         0
        .size:           144
        .value_kind:     by_value
    .group_segment_fixed_size: 16640
    .kernarg_segment_align: 8
    .kernarg_segment_size: 144
    .language:       OpenCL C
    .language_version:
      - 2
      - 0
    .max_flat_workgroup_size: 256
    .name:           _Z8prep_ln18PrepArgs
    .private_segment_fixed_size: 0
    .sgpr_count:     18
    .sgpr_spill_count: 0
    .symbol:         _Z8prep_ln18PrepArgs.kd
    .uniform_work_group_size: 1
    .uses_dynamic_stack: false
    .vgpr_count:     61
    .vgpr_spill_count: 0
    .wavefront_size: 64
  - .agpr_count:     0
    .args:
      - .address_space:  global
        .offset:         0
        .size:           8
        .value_kind:     global_buffer
      - .address_space:  global
        .offset:         8
        .size:           8
        .value_kind:     global_buffer
      - .address_space:  global
        .offset:         16
        .size:           8
        .value_kind:     global_buffer
      - .address_space:  global
        .offset:         24
        .size:           8
        .value_kind:     global_buffer
      - .offset:         32
        .size:           144
        .value_kind:     by_value
    .group_segment_fixed_size: 0
    .kernarg_segment_align: 8
    .kernarg_segment_size: 176
    .language:       OpenCL C
    .language_version:
      - 2
      - 0
    .max_flat_workgroup_size: 256
    .name:           _Z10attn64_fwdPKtS0_S0_Pt8PrepArgs
    .private_segment_fixed_size: 0
    .sgpr_count:     66
    .sgpr_spill_count: 0
    .symbol:         _Z10attn64_fwdPKtS0_S0_Pt8PrepArgs.kd
    .uniform_work_group_size: 1
    .uses_dynamic_stack: false
    .vgpr_count:     223
    .vgpr_spill_count: 0
    .wavefront_size: 64
  - .agpr_count:     0
    .args:
      - .address_space:  global
        .offset:         0
        .size:           8
        .value_kind:     global_buffer
      - .address_space:  global
        .offset:         8
        .size:           8
        .value_kind:     global_buffer
      - .offset:         16
        .size:           4
        .value_kind:     by_value
      - .offset:         20
        .size:           4
        .value_kind:     by_value
      - .offset:         24
        .size:           64
        .value_kind:     by_value
    .group_segment_fixed_size: 0
    .kernarg_segment_align: 8
    .kernarg_segment_size: 88
    .language:       OpenCL C
    .language_version:
      - 2
      - 0
    .max_flat_workgroup_size: 256
    .name:           _Z8gemm2b_kILi2EEvPKtS1_ii7EpiArgs
    .private_segment_fixed_size: 0
    .sgpr_count:     98
    .sgpr_spill_count: 0
    .symbol:         _Z8gemm2b_kILi2EEvPKtS1_ii7EpiArgs.kd
    .uniform_work_group_size: 1
    .uses_dynamic_stack: false
    .vgpr_count:     212
    .vgpr_spill_count: 0
    .wavefront_size: 64
  - .agpr_count:     0
    .args:
      - .address_space:  global
        .offset:         0
        .size:           8
        .value_kind:     global_buffer
      - .address_space:  global
        .offset:         8
        .size:           8
        .value_kind:     global_buffer
      - .offset:         16
        .size:           4
        .value_kind:     by_value
      - .offset:         20
        .size:           4
        .value_kind:     by_value
      - .offset:         24
        .size:           64
        .value_kind:     by_value
    .group_segment_fixed_size: 0
    .kernarg_segment_align: 8
    .kernarg_segment_size: 88
    .language:       OpenCL C
    .language_version:
      - 2
      - 0
    .max_flat_workgroup_size: 256
    .name:           _Z8gemm2b_kILi0EEvPKtS1_ii7EpiArgs
    .private_segment_fixed_size: 0
    .sgpr_count:     85
    .sgpr_spill_count: 0
    .symbol:         _Z8gemm2b_kILi0EEvPKtS1_ii7EpiArgs.kd
    .uniform_work_group_size: 1
    .uses_dynamic_stack: false
    .vgpr_count:     186
    .vgpr_spill_count: 0
    .wavefront_size: 64
  - .agpr_count:     0
    .args:
      - .address_space:  global
        .offset:         0
        .size:           8
        .value_kind:     global_buffer
      - .address_space:  global
        .offset:         8
        .size:           8
        .value_kind:     global_buffer
      - .offset:         16
        .size:           4
        .value_kind:     by_value
      - .offset:         20
        .size:           4
        .value_kind:     by_value
      - .offset:         24
        .size:           64
        .value_kind:     by_value
    .group_segment_fixed_size: 0
    .kernarg_segment_align: 8
    .kernarg_segment_size: 88
    .language:       OpenCL C
    .language_version:
      - 2
      - 0
    .max_flat_workgroup_size: 512
    .name:           _Z6gemm_kILi1ELb1ELb0ELb1ELb1ELb0EEvPKtS1_ii7EpiArgs
    .private_segment_fixed_size: 0
    .sgpr_count:     61
    .sgpr_spill_count: 0
    .symbol:         _Z6gemm_kILi1ELb1ELb0ELb1ELb1ELb0EEvPKtS1_ii7EpiArgs.kd
    .uniform_work_group_size: 1
    .uses_dynamic_stack: false
    .vgpr_count:     116
    .vgpr_spill_count: 0
    .wavefront_size: 64
  - .agpr_count:     0
    .args:
      - .address_space:  global
        .offset:         0
        .size:           8
        .value_kind:     global_buffer
      - .address_space:  global
        .offset:         8
        .size:           8
        .value_kind:     global_buffer
      - .offset:         16
        .size:           4
        .value_kind:     by_value
      - .offset:         20
        .size:           4
        .value_kind:     by_value
      - .offset:         24
        .size:           64
        .value_kind:     by_value
    .group_segment_fixed_size: 0
    .kernarg_segment_align: 8
    .kernarg_segment_size: 88
    .language:       OpenCL C
    .language_version:
      - 2
      - 0
    .max_flat_workgroup_size: 512
    .name:           _Z6gemm_kILi1ELb1ELb1ELb0ELb0ELb1EEvPKtS1_ii7EpiArgs
    .private_segment_fixed_size: 0
    .sgpr_count:     84
    .sgpr_spill_count: 0
    .symbol:         _Z6gemm_kILi1ELb1ELb1ELb0ELb0ELb1EEvPKtS1_ii7EpiArgs.kd
    .uniform_work_group_size: 1
    .uses_dynamic_stack: false
    .vgpr_count:     224
    .vgpr_spill_count: 0
    .wavefront_size: 64
